# MLA side-job tick: waits for its two weight loads counted (vmcnt 4/3) instead of draining the newer LDS-DMA pieces
# speedup vs baseline: 1.0221x; 1.0052x over previous
; #define LAS __attribute__((address_space(3)))
; DEV void sj_tick(const Params& p, int layer, SideJob& sj, LAS char* lds, int tid) {
;     ...
;     } else if (ph == 1) {
;         const int krow = tid >> 4, c4 = (tid & 15) * 4;
;         LAS float* t0 = tile + krow * 65 + c4; LAS float* t1 = t0 + 32 * 65;
;         t0[0] = sj.v0[0]; t0[1] = sj.v0[1]; t0[2] = sj.v0[2]; t0[3] = sj.v0[3]; t1[0] = sj.v1[0]; t1[1] = sj.v1[1]; t1[2] = sj.v1[2]; t1[3] = sj.v1[3];
.LBB0_823:
	v_add_u32_e32 v98, 0x2080, v194
	s_waitcnt vmcnt(4)
	ds_write2_b32 v194, v182, v183 offset1:1
	ds_write2_b32 v194, v184, v185 offset0:2 offset1:3
	s_waitcnt vmcnt(3)
	ds_write2_b32 v98, v186, v187 offset1:1
	v_add_u32_e32 v98, 0x2088, v194
	s_mov_b32 s21, s36
	s_mov_b32 s57, s33
	ds_write2_b32 v98, v188, v189 offset1:1
